# baseline (speedup 1.0000x reference)
.LBB0_3:
	v_lshlrev_b64 v[36:37], 1, v[32:33]
	v_lshl_add_u64 v[38:39], s[4:5], 0, v[36:37]
	s_mov_b32 s4, 0x800000
	s_waitcnt vmcnt(4)
	v_cvt_pk_f16_f32 v28, v28, v29
	v_cvt_pk_f16_f32 v29, v30, v31
	v_cvt_pk_f16_f32 v31, v22, v23
	s_waitcnt vmcnt(2)
	v_cvt_pk_f16_f32 v22, v16, v17
	v_add_co_u32_e32 v16, vcc, s4, v38
	v_cvt_pk_f16_f32 v30, v20, v21
	s_nop 0
	v_addc_co_u32_e32 v17, vcc, 0, v39, vcc
	v_cvt_pk_f16_f32 v20, v24, v25
	v_cvt_pk_f16_f32 v21, v26, v27
	v_cvt_pk_f16_f32 v23, v18, v19
	s_waitcnt vmcnt(0)
	v_cvt_pk_f16_f32 v8, v8, v9
	v_cvt_pk_f16_f32 v9, v10, v11
	v_cvt_pk_f16_f32 v10, v4, v5
	v_cvt_pk_f16_f32 v11, v6, v7
	v_lshl_add_u64 v[4:5], s[6:7], 0, v[36:37]
	s_andn2_b64 vcc, exec, s[8:9]
	global_store_dwordx4 v[38:39], v[28:31], off sc0 sc1
	global_store_dwordx4 v[16:17], v[20:23], off sc0 sc1
	global_store_dwordx4 v[4:5], v[8:11], off sc0 sc1
	s_cbranch_vccnz .LBB0_5
	v_lshl_add_u64 v[4:5], v[32:33], 1, s[6:7]
	v_add_co_u32_e32 v4, vcc, 0x800000, v4
	v_cvt_pk_f16_f32 v0, v35, v1
	v_cvt_pk_f16_f32 v1, v2, v3
	v_cvt_pk_f16_f32 v2, v12, v13
	v_cvt_pk_f16_f32 v3, v14, v15
	v_addc_co_u32_e32 v5, vcc, 0, v5, vcc
	global_store_dwordx4 v[4:5], v[0:3], off sc0 sc1
